# P5 top-8 selection: each wave/group max step as one v_max_f32_dpp instead of mov_dpp+2 max (fewer VALU ops), on top of v5
# baseline (speedup 1.0000x reference)
.LBB0_2087:
	v_lshl_add_u64 v[84:85], s[90:91], 0, v[82:83]
	global_load_dwordx4 v[42:45], v[84:85], off offset:-240
	global_load_dwordx4 v[46:49], v[84:85], off offset:-256
	v_lshl_add_u64 v[90:91], s[90:91], 0, v[80:81]
	v_add_co_u32_e32 v96, vcc, s56, v90
	global_load_dwordx4 v[120:123], v[84:85], off offset:-176
	global_load_dwordx4 v[124:127], v[84:85], off offset:-192
	global_load_dwordx4 v[128:131], v[84:85], off offset:-112
	global_load_dwordx4 v[132:135], v[84:85], off offset:-128
	global_load_dwordx4 v[136:139], v[84:85], off offset:-48
	global_load_dwordx4 v[140:143], v[84:85], off offset:-64
	global_load_dwordx4 v[34:37], v[84:85], off offset:16
	global_load_dwordx4 v[38:41], v[84:85], off
	v_addc_co_u32_e32 v97, vcc, 0, v91, vcc
	v_add_co_u32_e32 v92, vcc, s58, v90
	s_add_i32 s20, s20, -8
	s_nop 0
	v_addc_co_u32_e32 v93, vcc, 0, v91, vcc
	v_add_co_u32_e32 v94, vcc, s57, v90
	v_lshl_add_u64 v[80:81], v[80:81], 0, s[36:37]
	s_nop 0
	v_addc_co_u32_e32 v95, vcc, 0, v91, vcc
	v_add_co_u32_e32 v86, vcc, s59, v90
	s_cmp_eq_u32 s20, 0
	s_nop 0
	v_addc_co_u32_e32 v87, vcc, 0, v91, vcc
	global_load_dwordx4 v[144:147], v[92:93], off offset:-4096
	global_load_dwordx4 v[148:151], v[96:97], off offset:512
	global_load_dwordx4 v[152:155], v[86:87], off offset:-4096
	global_load_dwordx4 v[156:159], v[94:95], off offset:512
	global_load_dwordx4 v[160:163], v[96:97], off offset:2048
	global_load_dwordx4 v[164:167], v[92:93], off
	global_load_dwordx4 v[172:175], v[96:97], off offset:2560
	global_load_dwordx4 v[176:179], v[92:93], off offset:2560
	v_add_co_u32_e32 v98, vcc, s60, v90
	v_lshl_add_u64 v[82:83], v[82:83], 0, s[38:39]
	s_nop 0
	v_addc_co_u32_e32 v99, vcc, 0, v91, vcc
	v_add_co_u32_e32 v88, vcc, s62, v90
	s_waitcnt vmcnt(17)
	v_cvt_pk_bf16_f32 v170, v42, v43
	s_waitcnt vmcnt(16)
	v_cvt_pk_bf16_f32 v168, v46, v47
	v_cvt_pk_bf16_f32 v169, v48, v49
	v_cvt_pk_bf16_f32 v171, v44, v45
	v_lshlrev_b32_e32 v96, 16, v168
	v_and_b32_e32 v97, 0xffff0000, v168
	s_waitcnt vmcnt(7)
	v_mfma_f32_32x32x16_bf16 v[2:17], v[168:171], v[144:147], v[2:17]
	v_lshlrev_b32_e32 v180, 16, v169
	v_and_b32_e32 v181, 0xffff0000, v169
	v_lshlrev_b32_e32 v182, 16, v170
	v_and_b32_e32 v183, 0xffff0000, v170
	v_add_f32_e64 v46, v46, -v96
	v_add_f32_e64 v47, v47, -v97
	v_pk_add_f32 v[48:49], v[48:49], v[180:181] neg_lo:[0,1] neg_hi:[0,1]
	v_pk_add_f32 v[42:43], v[42:43], v[182:183] neg_lo:[0,1] neg_hi:[0,1]
	s_waitcnt vmcnt(6)
	v_mfma_f32_32x32x16_bf16 v[18:33], v[168:171], v[148:151], v[18:33]
	v_cvt_pk_bf16_f32 v46, v46, v47
	v_cvt_pk_bf16_f32 v47, v48, v49
	v_cvt_pk_bf16_f32 v48, v42, v43
	v_addc_co_u32_e32 v89, vcc, 0, v91, vcc
	s_waitcnt vmcnt(5)
	v_mfma_f32_32x32x16_bf16 v[2:17], v[168:171], v[152:155], v[2:17]
	v_lshlrev_b32_e32 v152, 16, v171
	v_and_b32_e32 v153, 0xffff0000, v171
	v_add_f32_e64 v44, v44, -v152
	v_add_f32_e64 v45, v45, -v153
	v_cvt_pk_bf16_f32 v49, v44, v45
	v_add_co_u32_e32 v44, vcc, s61, v90
	s_waitcnt vmcnt(4)
	v_mfma_f32_32x32x16_bf16 v[18:33], v[168:171], v[156:159], v[18:33]
	v_addc_co_u32_e32 v45, vcc, 0, v91, vcc
	v_mfma_f32_32x32x16_bf16 v[2:17], v[46:49], v[144:147], v[2:17]
	v_cvt_pk_bf16_f32 v144, v124, v125
	v_cvt_pk_bf16_f32 v145, v126, v127
	v_cvt_pk_bf16_f32 v146, v120, v121
	v_cvt_pk_bf16_f32 v147, v122, v123
	v_lshlrev_b32_e32 v42, 16, v144
	v_and_b32_e32 v43, 0xffff0000, v144
	v_pk_add_f32 v[42:43], v[124:125], v[42:43] neg_lo:[0,1] neg_hi:[0,1]
	v_mfma_f32_32x32x16_bf16 v[18:33], v[46:49], v[148:151], v[18:33]
	global_load_dwordx4 v[46:49], v[94:95], off offset:2048
	v_lshlrev_b32_e32 v148, 16, v145
	global_load_dwordx4 v[94:97], v[94:95], off offset:2560
	v_and_b32_e32 v149, 0xffff0000, v145
	v_lshlrev_b32_e32 v150, 16, v146
	v_and_b32_e32 v151, 0xffff0000, v146
	v_pk_add_f32 v[120:121], v[120:121], v[150:151] neg_lo:[0,1] neg_hi:[0,1]
	s_waitcnt vmcnt(5)
	v_mfma_f32_32x32x16_bf16 v[2:17], v[144:147], v[160:163], v[2:17]
	s_waitcnt vmcnt(3)
	v_mfma_f32_32x32x16_bf16 v[18:33], v[144:147], v[172:175], v[18:33]
	s_waitcnt vmcnt(1)
	v_mfma_f32_32x32x16_bf16 v[2:17], v[144:147], v[46:49], v[2:17]
	v_lshlrev_b32_e32 v46, 16, v147
	v_and_b32_e32 v47, 0xffff0000, v147
	v_add_f32_e64 v48, v126, -v148
	v_add_f32_e64 v49, v127, -v149
	v_add_f32_e64 v122, v122, -v46
	v_add_f32_e64 v123, v123, -v47
	v_cvt_pk_bf16_f32 v46, v42, v43
	v_cvt_pk_bf16_f32 v47, v48, v49
	v_cvt_pk_bf16_f32 v48, v120, v121
	s_waitcnt vmcnt(0)
	v_mfma_f32_32x32x16_bf16 v[18:33], v[144:147], v[94:97], v[18:33]
	global_load_dwordx4 v[94:97], v[92:93], off offset:512
	v_cvt_pk_bf16_f32 v49, v122, v123
	v_cvt_pk_bf16_f32 v120, v132, v133
	v_cvt_pk_bf16_f32 v121, v134, v135
	v_cvt_pk_bf16_f32 v122, v128, v129
	v_cvt_pk_bf16_f32 v123, v130, v131
	v_lshlrev_b32_e32 v42, 16, v120
	v_mfma_f32_32x32x16_bf16 v[2:17], v[46:49], v[160:163], v[2:17]
	v_and_b32_e32 v43, 0xffff0000, v120
	v_lshlrev_b32_e32 v148, 16, v122
	v_and_b32_e32 v149, 0xffff0000, v122
	v_add_f32_e64 v42, v132, -v42
	v_add_f32_e64 v43, v133, -v43
	v_mfma_f32_32x32x16_bf16 v[18:33], v[46:49], v[172:175], v[18:33]
	global_load_dwordx4 v[46:49], v[86:87], off
	global_load_dwordx4 v[124:127], v[92:93], off offset:2048
	global_load_dwordx4 v[144:147], v[86:87], off offset:512
	v_lshlrev_b32_e32 v92, 16, v121
	v_and_b32_e32 v93, 0xffff0000, v121
	v_mfma_f32_32x32x16_bf16 v[2:17], v[120:123], v[164:167], v[2:17]
	s_waitcnt vmcnt(3)
	v_mfma_f32_32x32x16_bf16 v[18:33], v[120:123], v[94:97], v[18:33]
	s_waitcnt vmcnt(2)
	v_mfma_f32_32x32x16_bf16 v[2:17], v[120:123], v[46:49], v[2:17]
	v_lshlrev_b32_e32 v46, 16, v123
	v_and_b32_e32 v47, 0xffff0000, v123
	v_add_f32_e64 v48, v134, -v92
	v_add_f32_e64 v49, v135, -v93
	v_add_f32_e64 v92, v128, -v148
	v_add_f32_e64 v93, v129, -v149
	v_pk_add_f32 v[128:129], v[130:131], v[46:47] neg_lo:[0,1] neg_hi:[0,1]
	v_cvt_pk_bf16_f32 v46, v42, v43
	v_add_co_u32_e32 v42, vcc, s63, v90
	s_waitcnt vmcnt(0)
	v_mfma_f32_32x32x16_bf16 v[18:33], v[120:123], v[144:147], v[18:33]
	v_cvt_pk_bf16_f32 v47, v48, v49
	v_cvt_pk_bf16_f32 v48, v92, v93
	v_addc_co_u32_e32 v43, vcc, 0, v91, vcc
	global_load_dwordx4 v[90:93], v[84:85], off offset:64
	global_load_dwordx4 v[120:123], v[86:87], off offset:2048
	v_cvt_pk_bf16_f32 v49, v128, v129
	v_cvt_pk_bf16_f32 v128, v140, v141
	v_cvt_pk_bf16_f32 v129, v142, v143
	v_mfma_f32_32x32x16_bf16 v[2:17], v[46:49], v[164:167], v[2:17]
	v_cvt_pk_bf16_f32 v130, v136, v137
	v_cvt_pk_bf16_f32 v131, v138, v139
	v_lshlrev_b32_e32 v132, 16, v129
	v_and_b32_e32 v133, 0xffff0000, v129
	v_lshlrev_b32_e32 v134, 16, v130
	v_and_b32_e32 v135, 0xffff0000, v130
	v_mfma_f32_32x32x16_bf16 v[18:33], v[46:49], v[94:97], v[18:33]
	global_load_dwordx4 v[46:49], v[86:87], off offset:2560
	global_load_dwordx4 v[94:97], v[88:89], off offset:-4096
	v_lshlrev_b32_e32 v86, 16, v128
	v_and_b32_e32 v87, 0xffff0000, v128
	v_add_f32_e64 v86, v140, -v86
	v_add_f32_e64 v87, v141, -v87
	v_mfma_f32_32x32x16_bf16 v[2:17], v[128:131], v[124:127], v[2:17]
	v_mfma_f32_32x32x16_bf16 v[18:33], v[128:131], v[176:179], v[18:33]
	s_waitcnt vmcnt(2)
	v_mfma_f32_32x32x16_bf16 v[2:17], v[128:131], v[120:123], v[2:17]
	v_lshlrev_b32_e32 v120, 16, v131
	v_and_b32_e32 v121, 0xffff0000, v131
	v_add_f32_e64 v122, v142, -v132
	v_add_f32_e64 v123, v143, -v133
	v_add_f32_e64 v132, v136, -v134
	v_add_f32_e64 v133, v137, -v135
	v_pk_add_f32 v[134:135], v[138:139], v[120:121] neg_lo:[0,1] neg_hi:[0,1]
	v_cvt_pk_bf16_f32 v120, v86, v87
	v_cvt_pk_bf16_f32 v121, v122, v123
	v_cvt_pk_bf16_f32 v122, v132, v133
	v_cvt_pk_bf16_f32 v123, v134, v135
	s_waitcnt vmcnt(1)
	v_mfma_f32_32x32x16_bf16 v[18:33], v[128:131], v[46:49], v[18:33]
	v_cvt_pk_bf16_f32 v132, v38, v39
	v_cvt_pk_bf16_f32 v133, v40, v41
	v_cvt_pk_bf16_f32 v134, v34, v35
	v_cvt_pk_bf16_f32 v135, v36, v37
	v_lshlrev_b32_e32 v86, 16, v132
	v_and_b32_e32 v87, 0xffff0000, v132
	v_lshlrev_b32_e32 v148, 16, v134
	v_mfma_f32_32x32x16_bf16 v[2:17], v[120:123], v[124:127], v[2:17]
	global_load_dwordx4 v[46:49], v[98:99], off offset:512
	global_load_dwordx4 v[124:127], v[42:43], off offset:-4096
	global_load_dwordx4 v[128:131], v[88:89], off
	v_and_b32_e32 v149, 0xffff0000, v134
	v_add_f32_e64 v38, v38, -v86
	v_add_f32_e64 v39, v39, -v87
	v_pk_add_f32 v[86:87], v[34:35], v[148:149] neg_lo:[0,1] neg_hi:[0,1]
	v_cvt_pk_bf16_f32 v34, v38, v39
	v_mfma_f32_32x32x16_bf16 v[18:33], v[120:123], v[176:179], v[18:33]
	global_load_dwordx4 v[120:123], v[44:45], off offset:512
	global_load_dwordx4 v[136:139], v[98:99], off offset:2048
	global_load_dwordx4 v[140:143], v[98:99], off offset:2560
	v_lshlrev_b32_e32 v98, 16, v133
	v_and_b32_e32 v99, 0xffff0000, v133
	v_pk_add_f32 v[40:41], v[40:41], v[98:99] neg_lo:[0,1] neg_hi:[0,1]
	global_load_dwordx4 v[144:147], v[88:89], off offset:2560
	v_cvt_pk_bf16_f32 v35, v40, v41
	s_waitcnt vmcnt(7)
	v_mfma_f32_32x32x16_bf16 v[2:17], v[132:135], v[94:97], v[2:17]
	s_waitcnt vmcnt(6)
	v_mfma_f32_32x32x16_bf16 v[18:33], v[132:135], v[46:49], v[18:33]
	s_waitcnt vmcnt(5)
	v_mfma_f32_32x32x16_bf16 v[2:17], v[132:135], v[124:127], v[2:17]
	v_lshlrev_b32_e32 v124, 16, v135
	v_and_b32_e32 v125, 0xffff0000, v135
	v_add_f32_e64 v98, v36, -v124
	v_add_f32_e64 v99, v37, -v125
	v_cvt_pk_bf16_f32 v36, v86, v87
	v_cvt_pk_bf16_f32 v37, v98, v99
	s_waitcnt vmcnt(3)
	v_mfma_f32_32x32x16_bf16 v[18:33], v[132:135], v[120:123], v[18:33]
	v_cvt_pk_bf16_f32 v132, v90, v91
	v_cvt_pk_bf16_f32 v133, v92, v93
	v_lshlrev_b32_e32 v86, 16, v133
	v_and_b32_e32 v87, 0xffff0000, v133
	v_mfma_f32_32x32x16_bf16 v[2:17], v[34:37], v[94:97], v[2:17]
	global_load_dwordx4 v[38:41], v[84:85], off offset:80
	global_load_dwordx4 v[94:97], v[84:85], off offset:144
	global_load_dwordx4 v[120:123], v[84:85], off offset:128
	global_load_dwordx4 v[124:127], v[84:85], off offset:192
	s_waitcnt vmcnt(3)
	v_cvt_pk_bf16_f32 v134, v38, v39
	v_mfma_f32_32x32x16_bf16 v[18:33], v[34:37], v[46:49], v[18:33]
	global_load_dwordx4 v[34:37], v[44:45], off offset:2048
	v_cvt_pk_bf16_f32 v135, v40, v41
	global_load_dwordx4 v[44:47], v[44:45], off offset:2560
	v_lshlrev_b32_e32 v48, 16, v132
	v_and_b32_e32 v49, 0xffff0000, v132
	v_lshlrev_b32_e32 v98, 16, v134
	v_and_b32_e32 v99, 0xffff0000, v134
	v_mfma_f32_32x32x16_bf16 v[2:17], v[132:135], v[136:139], v[2:17]
	v_add_f32_e64 v38, v38, -v98
	v_add_f32_e64 v39, v39, -v99
	v_mfma_f32_32x32x16_bf16 v[18:33], v[132:135], v[140:143], v[18:33]
	s_waitcnt vmcnt(1)
	v_mfma_f32_32x32x16_bf16 v[2:17], v[132:135], v[34:37], v[2:17]
	v_lshlrev_b32_e32 v34, 16, v135
	v_and_b32_e32 v35, 0xffff0000, v135
	v_add_f32_e64 v36, v90, -v48
	v_add_f32_e64 v37, v91, -v49
	v_add_f32_e64 v40, v40, -v34
	v_add_f32_e64 v41, v41, -v35
	v_cvt_pk_bf16_f32 v34, v36, v37
	v_cvt_pk_bf16_f32 v36, v38, v39
	v_cvt_pk_bf16_f32 v37, v40, v41
	global_load_dwordx4 v[38:41], v[88:89], off offset:512
	s_waitcnt vmcnt(1)
	v_mfma_f32_32x32x16_bf16 v[18:33], v[132:135], v[44:47], v[18:33]
	v_add_f32_e64 v48, v92, -v86
	v_add_f32_e64 v49, v93, -v87
	v_cvt_pk_bf16_f32 v44, v120, v121
	v_cvt_pk_bf16_f32 v35, v48, v49
	v_cvt_pk_bf16_f32 v45, v122, v123
	v_cvt_pk_bf16_f32 v46, v94, v95
	v_cvt_pk_bf16_f32 v47, v96, v97
	v_lshlrev_b32_e32 v48, 16, v44
	v_mfma_f32_32x32x16_bf16 v[2:17], v[34:37], v[136:139], v[2:17]
	v_and_b32_e32 v49, 0xffff0000, v44
	v_lshlrev_b32_e32 v98, 16, v45
	v_and_b32_e32 v99, 0xffff0000, v45
	v_lshlrev_b32_e32 v132, 16, v46
	v_and_b32_e32 v133, 0xffff0000, v46
	v_pk_add_f32 v[94:95], v[94:95], v[132:133] neg_lo:[0,1] neg_hi:[0,1]
	v_mfma_f32_32x32x16_bf16 v[18:33], v[34:37], v[140:143], v[18:33]
	global_load_dwordx4 v[34:37], v[42:43], off
	s_nop 0
	global_load_dwordx4 v[86:89], v[88:89], off offset:2048
	s_nop 0
	global_load_dwordx4 v[90:93], v[42:43], off offset:512
	v_mfma_f32_32x32x16_bf16 v[2:17], v[44:47], v[128:131], v[2:17]
	s_waitcnt vmcnt(3)
	v_mfma_f32_32x32x16_bf16 v[18:33], v[44:47], v[38:41], v[18:33]
	s_waitcnt vmcnt(2)
	v_mfma_f32_32x32x16_bf16 v[2:17], v[44:47], v[34:37], v[2:17]
	v_lshlrev_b32_e32 v34, 16, v47
	v_and_b32_e32 v35, 0xffff0000, v47
	v_add_f32_e64 v36, v120, -v48
	v_add_f32_e64 v37, v121, -v49
	v_add_f32_e64 v48, v122, -v98
	v_add_f32_e64 v49, v123, -v99
	v_pk_add_f32 v[96:97], v[96:97], v[34:35] neg_lo:[0,1] neg_hi:[0,1]
	v_cvt_pk_bf16_f32 v34, v36, v37
	v_cvt_pk_bf16_f32 v35, v48, v49
	s_waitcnt vmcnt(0)
	v_mfma_f32_32x32x16_bf16 v[18:33], v[44:47], v[90:93], v[18:33]
	global_load_dwordx4 v[44:47], v[84:85], off offset:208
	v_cvt_pk_bf16_f32 v36, v94, v95
	v_cvt_pk_bf16_f32 v37, v96, v97
	v_cvt_pk_bf16_f32 v90, v124, v125
	v_cvt_pk_bf16_f32 v91, v126, v127
	v_lshlrev_b32_e32 v48, 16, v91
	v_and_b32_e32 v49, 0xffff0000, v91
	v_mfma_f32_32x32x16_bf16 v[2:17], v[34:37], v[128:131], v[2:17]
	s_waitcnt vmcnt(0)
	v_cvt_pk_bf16_f32 v92, v44, v45
	v_mfma_f32_32x32x16_bf16 v[18:33], v[34:37], v[38:41], v[18:33]
	global_load_dwordx4 v[34:37], v[42:43], off offset:2048
	global_load_dwordx4 v[38:41], v[42:43], off offset:2560
	v_cvt_pk_bf16_f32 v93, v46, v47
	v_lshlrev_b32_e32 v42, 16, v90
	v_and_b32_e32 v43, 0xffff0000, v90
	v_lshlrev_b32_e32 v84, 16, v92
	v_and_b32_e32 v85, 0xffff0000, v92
	v_mfma_f32_32x32x16_bf16 v[2:17], v[90:93], v[86:89], v[2:17]
	v_add_f32_e64 v44, v44, -v84
	v_add_f32_e64 v45, v45, -v85
	v_mfma_f32_32x32x16_bf16 v[18:33], v[90:93], v[144:147], v[18:33]
	s_waitcnt vmcnt(1)
	v_mfma_f32_32x32x16_bf16 v[2:17], v[90:93], v[34:37], v[2:17]
	v_lshlrev_b32_e32 v34, 16, v93
	v_and_b32_e32 v35, 0xffff0000, v93
	v_add_f32_e64 v36, v124, -v42
	v_add_f32_e64 v37, v125, -v43
	v_add_f32_e64 v42, v126, -v48
	v_add_f32_e64 v43, v127, -v49
	v_pk_add_f32 v[46:47], v[46:47], v[34:35] neg_lo:[0,1] neg_hi:[0,1]
	v_cvt_pk_bf16_f32 v34, v36, v37
	v_cvt_pk_bf16_f32 v35, v42, v43
	s_waitcnt vmcnt(0)
	v_mfma_f32_32x32x16_bf16 v[18:33], v[90:93], v[38:41], v[18:33]
	v_cvt_pk_bf16_f32 v36, v44, v45
	v_cvt_pk_bf16_f32 v37, v46, v47
	s_nop 1
	v_mfma_f32_32x32x16_bf16 v[2:17], v[34:37], v[86:89], v[2:17]
	v_mfma_f32_32x32x16_bf16 v[18:33], v[34:37], v[144:147], v[18:33]
	s_cbranch_scc0 .LBB0_2087
	v_add_u32_e32 v1, 0x800, v114
	s_nop 9
	ds_write2_b32 v114, v2, v18 offset1:32
	ds_write2_b32 v114, v3, v19 offset0:64 offset1:96
	ds_write2_b32 v114, v4, v20 offset0:128 offset1:160
	ds_write2_b32 v114, v5, v21 offset0:192 offset1:224
	ds_write2_b32 v1, v6, v22 offset1:32
	ds_write2_b32 v1, v7, v23 offset0:64 offset1:96
	ds_write2_b32 v1, v8, v24 offset0:128 offset1:160
	ds_write2_b32 v1, v9, v25 offset0:192 offset1:224
	v_add_u32_e32 v1, 0x1000, v114
	ds_write2_b32 v1, v10, v26 offset1:32
	ds_write2_b32 v1, v11, v27 offset0:64 offset1:96
	ds_write2_b32 v1, v12, v28 offset0:128 offset1:160
	ds_write2_b32 v1, v13, v29 offset0:192 offset1:224
	v_add_u32_e32 v1, 0x1800, v114
	ds_write2_b32 v1, v14, v30 offset1:32
	ds_write2_b32 v1, v15, v31 offset0:64 offset1:96
	ds_write2_b32 v1, v16, v32 offset0:128 offset1:160
	ds_write2_b32 v1, v17, v33 offset0:192 offset1:224
	s_waitcnt lgkmcnt(0)
	s_barrier
	ds_read2st64_b32 v[2:3], v104 offset1:8
	ds_read2st64_b32 v[4:5], v104 offset0:32 offset1:40
	ds_read2st64_b32 v[6:7], v104 offset0:64 offset1:72
	ds_read2st64_b32 v[8:9], v104 offset0:96 offset1:104
	ds_read2st64_b32 v[10:11], v104 offset0:128 offset1:136
	ds_read2st64_b32 v[12:13], v104 offset0:160 offset1:168
	ds_read2st64_b32 v[14:15], v104 offset0:192 offset1:200
	s_waitcnt lgkmcnt(6)
	v_add_f32_e32 v1, 0, v2
	s_waitcnt lgkmcnt(5)
	v_add_f32_e32 v1, v1, v4
	s_waitcnt lgkmcnt(4)
	v_add_f32_e32 v1, v1, v6
	ds_read2st64_b32 v[16:17], v104 offset0:224 offset1:232
	s_waitcnt lgkmcnt(4)
	v_add_f32_e32 v1, v1, v8
	ds_read_b32 v2, v105
	s_waitcnt lgkmcnt(4)
	v_add_f32_e32 v1, v1, v10
	s_waitcnt lgkmcnt(3)
	v_add_f32_e32 v1, v1, v12
	s_waitcnt lgkmcnt(2)
	v_add_f32_e32 v1, v1, v14
	s_waitcnt lgkmcnt(1)
	v_add_f32_e32 v1, v1, v16
	s_waitcnt lgkmcnt(0)
	v_mul_f32_e32 v1, v1, v2
	ds_read_b32 v8, v107
	ds_read_b32 v18, v109
	ds_read_b32 v19, v111
	ds_write_b32 v106, v1
	v_add_f32_e32 v1, 0, v3
	v_add_f32_e32 v1, v1, v5
	v_add_f32_e32 v1, v1, v7
	v_add_f32_e32 v1, v1, v9
	v_add_f32_e32 v1, v1, v11
	v_add_f32_e32 v1, v1, v13
	v_add_f32_e32 v1, v1, v15
	ds_read2st64_b32 v[2:3], v104 offset0:16 offset1:24
	ds_read2st64_b32 v[4:5], v104 offset0:48 offset1:56
	ds_read2st64_b32 v[6:7], v104 offset0:80 offset1:88
	v_add_f32_e32 v1, v1, v17
	s_waitcnt lgkmcnt(6)
	v_mul_f32_e32 v1, v1, v8
	ds_write_b32 v108, v1
	s_waitcnt lgkmcnt(3)
	v_add_f32_e32 v1, 0, v2
	s_waitcnt lgkmcnt(2)
	v_add_f32_e32 v1, v1, v4
	s_waitcnt lgkmcnt(1)
	v_add_f32_e32 v1, v1, v6
	ds_read2st64_b32 v[8:9], v104 offset0:112 offset1:120
	ds_read2st64_b32 v[10:11], v104 offset0:144 offset1:152
	ds_read2st64_b32 v[12:13], v104 offset0:176 offset1:184
	ds_read2st64_b32 v[14:15], v104 offset0:208 offset1:216
	ds_read2st64_b32 v[16:17], v104 offset0:240 offset1:248
	s_waitcnt lgkmcnt(4)
	v_add_f32_e32 v1, v1, v8
	s_waitcnt lgkmcnt(3)
	v_add_f32_e32 v1, v1, v10
	s_waitcnt lgkmcnt(2)
	v_add_f32_e32 v1, v1, v12
	s_waitcnt lgkmcnt(1)
	v_add_f32_e32 v1, v1, v14
	s_waitcnt lgkmcnt(0)
	v_add_f32_e32 v1, v1, v16
	v_mul_f32_e32 v1, v1, v18
	ds_write_b32 v110, v1
	v_add_f32_e32 v1, 0, v3
	v_add_f32_e32 v1, v1, v5
	v_add_f32_e32 v1, v1, v7
	v_add_f32_e32 v1, v1, v9
	v_add_f32_e32 v1, v1, v11
	v_add_f32_e32 v1, v1, v13
	v_add_f32_e32 v1, v1, v15
	v_add_f32_e32 v1, v1, v17
	v_mul_f32_e32 v1, v1, v19
	ds_write_b32 v112, v1
	s_waitcnt lgkmcnt(0)
	s_barrier
	global_load_dword v3, v[60:61], off
	ds_read_b32 v1, v119
	s_waitcnt lgkmcnt(0)
	v_mul_f32_e32 v1, 0xbfb8aa3b, v1
	v_exp_f32_e32 v1, v1
	s_nop 0
	v_add_f32_e32 v1, 1.0, v1
	v_div_scale_f32 v2, s[20:21], v1, v1, 1.0
	v_rcp_f32_e32 v4, v2
	s_nop 0
	v_fma_f32 v5, -v2, v4, 1.0
	v_fmac_f32_e32 v4, v5, v4
	v_div_scale_f32 v5, vcc, 1.0, v1, 1.0
	v_mul_f32_e32 v6, v5, v4
	v_fma_f32 v7, -v2, v6, v5
	v_fmac_f32_e32 v6, v7, v4
	v_fma_f32 v2, -v2, v6, v5
	v_div_fmas_f32 v2, v2, v4, v6
	v_div_fixup_f32 v5, v2, v1, 1.0
	s_waitcnt vmcnt(0)
	v_add_f32_e32 v1, v3, v5
	s_nop 1
	v_max_f32_dpp v2, v1, v1 quad_perm:[1,0,3,2] row_mask:0xf bank_mask:0xf bound_ctrl:1
	s_nop 1
	v_max_f32_dpp v2, v2, v2 quad_perm:[2,3,0,1] row_mask:0xf bank_mask:0xf bound_ctrl:1
	s_nop 1
	v_max_f32_dpp v2, v2, v2 row_half_mirror row_mask:0xf bank_mask:0xf bound_ctrl:1
	v_cmp_eq_f32_e32 vcc, v1, v2
	s_nop 1
	v_and_b32_e32 v4, vcc_hi, v63
	v_and_b32_e32 v6, vcc_lo, v62
	v_ffbl_b32_e32 v4, v4
	v_add_u32_e32 v4, 32, v4
	v_ffbl_b32_e32 v6, v6
	v_min_u32_e32 v4, v6, v4
	v_cmp_ne_u32_e32 vcc, v198, v4
	s_nop 1
	v_cndmask_b32_e32 v4, v115, v1, vcc
	s_nop 1
	v_max_f32_dpp v4, v4, v4 quad_perm:[1,0,3,2] row_mask:0xf bank_mask:0xf bound_ctrl:1
	s_nop 1
	v_max_f32_dpp v4, v4, v4 quad_perm:[2,3,0,1] row_mask:0xf bank_mask:0xf bound_ctrl:1
	s_nop 1
	v_max_f32_dpp v4, v4, v4 row_half_mirror row_mask:0xf bank_mask:0xf bound_ctrl:1
	v_add_f32_e32 v2, v2, v4
	s_nop 0
	v_readlane_b32 s20, v2, 0
	s_nop 1
	v_cmp_gt_f32_e32 vcc, s20, v2
	v_cmp_eq_f32_e64 s[20:21], s20, v2
	s_and_b64 s[20:21], s[20:21], s[6:7]
	s_or_b64 s[20:21], vcc, s[20:21]
	v_cndmask_b32_e64 v4, 0, 1, s[20:21]
	v_readlane_b32 s20, v2, 8
	s_nop 1
	v_cmp_gt_f32_e32 vcc, s20, v2
	v_cmp_eq_f32_e64 s[20:21], s20, v2
	s_and_b64 s[20:21], s[20:21], s[8:9]
	s_or_b64 s[20:21], vcc, s[20:21]
	v_cndmask_b32_e64 v6, 0, 1, s[20:21]
	v_readlane_b32 s20, v2, 16
	s_nop 1
	v_cmp_gt_f32_e32 vcc, s20, v2
	v_cmp_eq_f32_e64 s[20:21], s20, v2
	s_and_b64 s[20:21], s[20:21], s[10:11]
	s_or_b64 s[20:21], vcc, s[20:21]
	v_cndmask_b32_e64 v7, 0, 1, s[20:21]
	v_readlane_b32 s20, v2, 24
	v_add3_u32 v4, v4, v6, v7
	s_nop 0
	v_cmp_gt_f32_e32 vcc, s20, v2
	v_cmp_eq_f32_e64 s[20:21], s20, v2
	s_and_b64 s[20:21], s[20:21], s[12:13]
	s_or_b64 s[20:21], vcc, s[20:21]
	v_cndmask_b32_e64 v6, 0, 1, s[20:21]
	v_readlane_b32 s20, v2, 32
	s_nop 1
	v_cmp_gt_f32_e32 vcc, s20, v2
	v_cmp_eq_f32_e64 s[20:21], s20, v2
	s_and_b64 s[20:21], s[20:21], s[14:15]
	s_or_b64 s[20:21], vcc, s[20:21]
	v_cndmask_b32_e64 v7, 0, 1, s[20:21]
	v_readlane_b32 s20, v2, 40
	v_add3_u32 v4, v4, v6, v7
	s_nop 0
	v_cmp_gt_f32_e32 vcc, s20, v2
	v_cmp_eq_f32_e64 s[20:21], s20, v2
	s_and_b64 s[20:21], s[20:21], s[16:17]
	s_or_b64 s[20:21], vcc, s[20:21]
	v_cndmask_b32_e64 v6, 0, 1, s[20:21]
	v_readlane_b32 s20, v2, 48
	s_nop 1
	v_cmp_gt_f32_e32 vcc, s20, v2
	v_cmp_eq_f32_e64 s[20:21], s20, v2
	s_and_b64 s[20:21], s[18:19], s[20:21]
	s_or_b64 s[20:21], vcc, s[20:21]
	v_cndmask_b32_e64 v7, 0, 1, s[20:21]
	v_readlane_b32 s20, v2, 56
	s_nop 1
	v_cmp_gt_f32_e32 vcc, s20, v2
	s_nop 1
	v_addc_co_u32_e32 v2, vcc, v4, v6, vcc
	v_add_u32_e32 v2, v2, v7
	v_cmp_gt_u32_e32 vcc, 4, v2
	s_nop 0
	s_nop 0
	v_cndmask_b32_e32 v1, v115, v1, vcc
	s_nop 0
	v_mov_b32_e32 v2, v1
	v_max_f32_dpp v2, v1, v2 row_shr:1 row_mask:0xf bank_mask:0xf
	s_nop 1
	v_max_f32_dpp v2, v2, v2 row_shr:2 row_mask:0xf bank_mask:0xf
	s_nop 1
	v_max_f32_dpp v2, v2, v2 row_shr:4 row_mask:0xf bank_mask:0xf
	s_nop 1
	v_max_f32_dpp v2, v2, v2 row_shr:8 row_mask:0xf bank_mask:0xf
	s_nop 1
	v_max_f32_dpp v2, v2, v2 row_bcast:15 row_mask:0xa bank_mask:0xf
	s_nop 1
	v_max_f32_dpp v2, v2, v2 row_bcast:31 row_mask:0xc bank_mask:0xf
	s_nop 0
	v_readlane_b32 s20, v2, 63
	s_nop 1
	v_cmp_eq_f32_e32 vcc, s20, v1
	s_ff1_i32_b64 s20, vcc
	v_cmp_ne_u32_e32 vcc, s20, v198
	s_nop 1
	v_cndmask_b32_e32 v1, v115, v1, vcc
	v_cndmask_b32_e64 v2, 0, -1, vcc
	s_nop 0
	v_mov_b32_e32 v4, v1
	v_max_f32_dpp v4, v1, v4 row_shr:1 row_mask:0xf bank_mask:0xf
	s_nop 1
	v_max_f32_dpp v4, v4, v4 row_shr:2 row_mask:0xf bank_mask:0xf
	s_nop 1
	v_max_f32_dpp v4, v4, v4 row_shr:4 row_mask:0xf bank_mask:0xf
	s_nop 1
	v_max_f32_dpp v4, v4, v4 row_shr:8 row_mask:0xf bank_mask:0xf
	s_nop 1
	v_max_f32_dpp v4, v4, v4 row_bcast:15 row_mask:0xa bank_mask:0xf
	s_nop 1
	v_max_f32_dpp v4, v4, v4 row_bcast:31 row_mask:0xc bank_mask:0xf
	s_nop 0
	v_readlane_b32 s20, v4, 63
	s_nop 0
	s_nop 0
	v_cmp_eq_f32_e32 vcc, s20, v1
	s_ff1_i32_b64 s20, vcc
	v_cmp_eq_u32_e32 vcc, s20, v198
	s_nop 1
	v_cndmask_b32_e32 v1, v1, v115, vcc
	v_cndmask_b32_e64 v2, v2, 1, vcc
	s_nop 0
	v_mov_b32_e32 v4, v1
	v_max_f32_dpp v4, v1, v4 row_shr:1 row_mask:0xf bank_mask:0xf
	s_nop 1
	v_max_f32_dpp v4, v4, v4 row_shr:2 row_mask:0xf bank_mask:0xf
	s_nop 1
	v_max_f32_dpp v4, v4, v4 row_shr:4 row_mask:0xf bank_mask:0xf
	s_nop 1
	v_max_f32_dpp v4, v4, v4 row_shr:8 row_mask:0xf bank_mask:0xf
	s_nop 1
	v_max_f32_dpp v4, v4, v4 row_bcast:15 row_mask:0xa bank_mask:0xf
	s_nop 1
	v_max_f32_dpp v4, v4, v4 row_bcast:31 row_mask:0xc bank_mask:0xf
	s_nop 0
	v_readlane_b32 s20, v4, 63
	s_nop 0
	s_nop 0
	v_cmp_eq_f32_e32 vcc, s20, v1
	s_ff1_i32_b64 s20, vcc
	v_cmp_eq_u32_e32 vcc, s20, v198
	s_nop 1
	v_cndmask_b32_e32 v1, v1, v115, vcc
	v_cndmask_b32_e64 v2, v2, 2, vcc
	s_nop 0
	v_mov_b32_e32 v4, v1
	v_max_f32_dpp v4, v1, v4 row_shr:1 row_mask:0xf bank_mask:0xf
	s_nop 1
	v_max_f32_dpp v4, v4, v4 row_shr:2 row_mask:0xf bank_mask:0xf
	s_nop 1
	v_max_f32_dpp v4, v4, v4 row_shr:4 row_mask:0xf bank_mask:0xf
	s_nop 1
	v_max_f32_dpp v4, v4, v4 row_shr:8 row_mask:0xf bank_mask:0xf
	s_nop 1
	v_max_f32_dpp v4, v4, v4 row_bcast:15 row_mask:0xa bank_mask:0xf
	s_nop 1
	v_max_f32_dpp v4, v4, v4 row_bcast:31 row_mask:0xc bank_mask:0xf
	s_nop 0
	v_readlane_b32 s20, v4, 63
	s_nop 0
	s_nop 0
	v_cmp_eq_f32_e32 vcc, s20, v1
	s_ff1_i32_b64 s20, vcc
	v_cmp_eq_u32_e32 vcc, s20, v198
	s_nop 1
	v_cndmask_b32_e32 v1, v1, v115, vcc
	v_cndmask_b32_e64 v2, v2, 3, vcc
	s_nop 0
	v_mov_b32_e32 v4, v1
	v_max_f32_dpp v4, v1, v4 row_shr:1 row_mask:0xf bank_mask:0xf
	s_nop 1
	v_max_f32_dpp v4, v4, v4 row_shr:2 row_mask:0xf bank_mask:0xf
	s_nop 1
	v_max_f32_dpp v4, v4, v4 row_shr:4 row_mask:0xf bank_mask:0xf
	s_nop 1
	v_max_f32_dpp v4, v4, v4 row_shr:8 row_mask:0xf bank_mask:0xf
	s_nop 1
	v_max_f32_dpp v4, v4, v4 row_bcast:15 row_mask:0xa bank_mask:0xf
	s_nop 1
	v_max_f32_dpp v4, v4, v4 row_bcast:31 row_mask:0xc bank_mask:0xf
	s_nop 0
	v_readlane_b32 s20, v4, 63
	v_mov_b32_e32 v4, 0xff800000
	s_nop 0
	v_cmp_eq_f32_e32 vcc, s20, v1
	s_ff1_i32_b64 s20, vcc
	v_cmp_eq_u32_e32 vcc, s20, v198
	s_nop 1
	v_cndmask_b32_e32 v1, v1, v115, vcc
	v_max_f32_e32 v6, v1, v1
	v_cndmask_b32_e64 v2, v2, 4, vcc
	v_mov_b32_dpp v4, v1 row_shr:1 row_mask:0xf bank_mask:0xf
	v_max_f32_e32 v4, v4, v4
	v_max_f32_e32 v4, v6, v4
	s_nop 1
	v_max_f32_dpp v4, v4, v4 row_shr:2 row_mask:0xf bank_mask:0xf
	s_nop 1
	v_max_f32_dpp v4, v4, v4 row_shr:4 row_mask:0xf bank_mask:0xf
	s_nop 1
	v_max_f32_dpp v4, v4, v4 row_shr:8 row_mask:0xf bank_mask:0xf
	s_nop 1
	v_max_f32_dpp v4, v4, v4 row_bcast:15 row_mask:0xa bank_mask:0xf
	s_nop 1
	v_max_f32_dpp v4, v4, v4 row_bcast:31 row_mask:0xc bank_mask:0xf
	s_nop 0
	v_readlane_b32 s20, v4, 63
	v_mov_b32_e32 v4, 0xff800000
	s_nop 0
	v_cmp_eq_f32_e32 vcc, s20, v1
	s_ff1_i32_b64 s20, vcc
	v_cmp_eq_u32_e32 vcc, s20, v198
	s_nop 1
	v_cndmask_b32_e32 v1, v1, v115, vcc
	v_max_f32_e32 v6, v1, v1
	v_cndmask_b32_e64 v2, v2, 5, vcc
	v_mov_b32_dpp v4, v1 row_shr:1 row_mask:0xf bank_mask:0xf
	v_max_f32_e32 v4, v4, v4
	v_max_f32_e32 v4, v6, v4
	s_nop 1
	v_max_f32_dpp v4, v4, v4 row_shr:2 row_mask:0xf bank_mask:0xf
	s_nop 1
	v_max_f32_dpp v4, v4, v4 row_shr:4 row_mask:0xf bank_mask:0xf
	s_nop 1
	v_max_f32_dpp v4, v4, v4 row_shr:8 row_mask:0xf bank_mask:0xf
	s_nop 1
	v_max_f32_dpp v4, v4, v4 row_bcast:15 row_mask:0xa bank_mask:0xf
	s_nop 1
	v_max_f32_dpp v4, v4, v4 row_bcast:31 row_mask:0xc bank_mask:0xf
	s_nop 0
	v_readlane_b32 s20, v4, 63
	v_mov_b32_e32 v4, 0xff800000
	s_nop 0
	v_cmp_eq_f32_e32 vcc, s20, v1
	s_ff1_i32_b64 s20, vcc
	v_cmp_eq_u32_e32 vcc, s20, v198
	s_nop 1
	v_cndmask_b32_e32 v1, v1, v115, vcc
	v_max_f32_e32 v6, v1, v1
	v_cndmask_b32_e64 v2, v2, 6, vcc
	v_mov_b32_dpp v4, v1 row_shr:1 row_mask:0xf bank_mask:0xf
	v_max_f32_e32 v4, v4, v4
	v_max_f32_e32 v4, v6, v4
	s_nop 1
	v_max_f32_dpp v4, v4, v4 row_shr:2 row_mask:0xf bank_mask:0xf
	s_nop 1
	v_max_f32_dpp v4, v4, v4 row_shr:4 row_mask:0xf bank_mask:0xf
	s_nop 1
	v_max_f32_dpp v4, v4, v4 row_shr:8 row_mask:0xf bank_mask:0xf
	s_nop 1
	v_max_f32_dpp v4, v4, v4 row_bcast:15 row_mask:0xa bank_mask:0xf
	s_nop 1
	v_max_f32_dpp v4, v4, v4 row_bcast:31 row_mask:0xc bank_mask:0xf
	s_nop 0
	v_readlane_b32 s20, v4, 63
	s_nop 1
	v_cmp_eq_f32_e32 vcc, s20, v1
	s_ff1_i32_b64 s20, vcc
	v_cmp_ne_u32_e32 vcc, s20, v198
	s_nop 1
	v_cndmask_b32_e32 v6, 7, v2, vcc
	v_cmp_lt_i32_e64 s[20:21], -1, v6
	v_mov_b32_e32 v2, 0
	s_nop 0
	v_cndmask_b32_e64 v1, 0, v5, s[20:21]
	s_nop 1
	v_add_f32_dpp v1, v1, v1 row_shr:1 row_mask:0xf bank_mask:0xf bound_ctrl:1
	s_nop 1
	v_add_f32_dpp v1, v1, v1 row_shr:2 row_mask:0xf bank_mask:0xf bound_ctrl:1
	s_nop 1
	v_add_f32_dpp v1, v1, v1 row_shr:4 row_mask:0xf bank_mask:0xf bound_ctrl:1
	s_nop 1
	v_add_f32_dpp v1, v1, v1 row_shr:8 row_mask:0xf bank_mask:0xf bound_ctrl:1
	s_nop 1
	v_mov_b32_dpp v2, v1 row_bcast:15 row_mask:0xa bank_mask:0xf
	v_add_f32_e32 v1, v1, v2
	v_mov_b32_e32 v2, 0
	s_nop 1
	v_mov_b32_dpp v2, v1 row_bcast:31 row_mask:0xc bank_mask:0xf
	v_add_f32_e32 v1, v1, v2
	v_mov_b32_e32 v2, s35
	v_readlane_b32 s41, v1, 63
	s_and_saveexec_b64 s[22:23], s[20:21]
	ds_add_rtn_u32 v2, v101, v116
	s_or_b64 exec, exec, s[22:23]
	ds_read_b32 v1, v119 offset:256
	s_waitcnt lgkmcnt(0)
	v_mul_f32_e32 v1, 0xbfb8aa3b, v1
	v_exp_f32_e32 v1, v1
	s_nop 0
	v_add_f32_e32 v1, 1.0, v1
	v_div_scale_f32 v4, s[22:23], v1, v1, 1.0
	v_rcp_f32_e32 v7, v4
	v_div_scale_f32 v8, vcc, 1.0, v1, 1.0
	v_fma_f32 v9, -v4, v7, 1.0
	v_fmac_f32_e32 v7, v9, v7
	v_mul_f32_e32 v9, v8, v7
	v_fma_f32 v10, -v4, v9, v8
	v_fmac_f32_e32 v9, v10, v7
	v_fma_f32 v4, -v4, v9, v8
	v_div_fmas_f32 v4, v4, v7, v9
	v_div_fixup_f32 v7, v4, v1, 1.0
	v_add_f32_e32 v1, v3, v7
	s_nop 1
	v_max_f32_dpp v4, v1, v1 quad_perm:[1,0,3,2] row_mask:0xf bank_mask:0xf bound_ctrl:1
	s_nop 1
	v_max_f32_dpp v4, v4, v4 quad_perm:[2,3,0,1] row_mask:0xf bank_mask:0xf bound_ctrl:1
	s_nop 1
	v_max_f32_dpp v4, v4, v4 row_half_mirror row_mask:0xf bank_mask:0xf bound_ctrl:1
	v_cmp_eq_f32_e32 vcc, v1, v4
	s_nop 1
	v_and_b32_e32 v8, vcc_hi, v63
	v_and_b32_e32 v9, vcc_lo, v62
	v_ffbl_b32_e32 v8, v8
	v_ffbl_b32_e32 v9, v9
	v_add_u32_e32 v8, 32, v8
	v_min_u32_e32 v8, v9, v8
	v_cmp_ne_u32_e32 vcc, v198, v8
	s_nop 1
	v_cndmask_b32_e32 v8, v115, v1, vcc
	s_nop 1
	v_max_f32_dpp v8, v8, v8 quad_perm:[1,0,3,2] row_mask:0xf bank_mask:0xf bound_ctrl:1
	s_nop 1
	v_max_f32_dpp v8, v8, v8 quad_perm:[2,3,0,1] row_mask:0xf bank_mask:0xf bound_ctrl:1
	s_nop 1
	v_max_f32_dpp v8, v8, v8 row_half_mirror row_mask:0xf bank_mask:0xf bound_ctrl:1
	v_add_f32_e32 v4, v4, v8
	s_nop 0
	v_readlane_b32 s22, v4, 0
	v_readlane_b32 s24, v4, 8
	s_nop 0
	v_cmp_gt_f32_e32 vcc, s22, v4
	v_cmp_eq_f32_e64 s[22:23], s22, v4
	s_and_b64 s[22:23], s[22:23], s[6:7]
	s_or_b64 s[22:23], vcc, s[22:23]
	v_cndmask_b32_e64 v8, 0, 1, s[22:23]
	v_cmp_eq_f32_e64 s[22:23], s24, v4
	v_cmp_gt_f32_e32 vcc, s24, v4
	s_and_b64 s[22:23], s[22:23], s[8:9]
	s_or_b64 s[22:23], vcc, s[22:23]
	v_cndmask_b32_e64 v9, 0, 1, s[22:23]
	v_readlane_b32 s22, v4, 16
	s_nop 1
	v_cmp_gt_f32_e32 vcc, s22, v4
	v_cmp_eq_f32_e64 s[22:23], s22, v4
	s_and_b64 s[22:23], s[22:23], s[10:11]
	s_or_b64 s[22:23], vcc, s[22:23]
	v_cndmask_b32_e64 v10, 0, 1, s[22:23]
	v_readlane_b32 s22, v4, 24
	v_add3_u32 v8, v8, v9, v10
	s_nop 0
	v_cmp_gt_f32_e32 vcc, s22, v4
	v_cmp_eq_f32_e64 s[22:23], s22, v4
	s_and_b64 s[22:23], s[22:23], s[12:13]
	s_or_b64 s[22:23], vcc, s[22:23]
	v_cndmask_b32_e64 v9, 0, 1, s[22:23]
	v_readlane_b32 s22, v4, 32
	s_nop 1
	v_cmp_gt_f32_e32 vcc, s22, v4
	v_cmp_eq_f32_e64 s[22:23], s22, v4
	s_and_b64 s[22:23], s[22:23], s[14:15]
	s_or_b64 s[22:23], vcc, s[22:23]
	v_cndmask_b32_e64 v10, 0, 1, s[22:23]
	v_readlane_b32 s22, v4, 40
	v_add3_u32 v8, v8, v9, v10
	s_nop 0
	v_cmp_gt_f32_e32 vcc, s22, v4
	v_cmp_eq_f32_e64 s[22:23], s22, v4
	s_and_b64 s[22:23], s[22:23], s[16:17]
	s_or_b64 s[22:23], vcc, s[22:23]
	v_cndmask_b32_e64 v9, 0, 1, s[22:23]
	v_readlane_b32 s22, v4, 48
	s_nop 1
	v_cmp_gt_f32_e32 vcc, s22, v4
	v_cmp_eq_f32_e64 s[22:23], s22, v4
	s_and_b64 s[22:23], s[18:19], s[22:23]
	s_or_b64 s[22:23], vcc, s[22:23]
	v_cndmask_b32_e64 v10, 0, 1, s[22:23]
	v_readlane_b32 s22, v4, 56
	s_nop 1
	v_cmp_gt_f32_e32 vcc, s22, v4
	s_nop 1
	v_addc_co_u32_e32 v4, vcc, v8, v9, vcc
	v_add_u32_e32 v4, v4, v10
	v_cmp_gt_u32_e32 vcc, 4, v4
	s_nop 0
	s_nop 0
	v_cndmask_b32_e32 v1, v115, v1, vcc
	s_nop 0
	v_mov_b32_e32 v4, v1
	v_max_f32_dpp v4, v1, v4 row_shr:1 row_mask:0xf bank_mask:0xf
	s_nop 1
	v_max_f32_dpp v4, v4, v4 row_shr:2 row_mask:0xf bank_mask:0xf
	s_nop 1
	v_max_f32_dpp v4, v4, v4 row_shr:4 row_mask:0xf bank_mask:0xf
	s_nop 1
	v_max_f32_dpp v4, v4, v4 row_shr:8 row_mask:0xf bank_mask:0xf
	s_nop 1
	v_max_f32_dpp v4, v4, v4 row_bcast:15 row_mask:0xa bank_mask:0xf
	s_nop 1
	v_max_f32_dpp v4, v4, v4 row_bcast:31 row_mask:0xc bank_mask:0xf
	s_nop 0
	v_readlane_b32 s22, v4, 63
	s_nop 1
	v_cmp_eq_f32_e32 vcc, s22, v1
	s_ff1_i32_b64 s22, vcc
	v_cmp_ne_u32_e32 vcc, s22, v198
	s_nop 1
	v_cndmask_b32_e32 v1, v115, v1, vcc
	v_cndmask_b32_e64 v4, 0, -1, vcc
	s_nop 0
	v_mov_b32_e32 v8, v1
	v_max_f32_dpp v8, v1, v8 row_shr:1 row_mask:0xf bank_mask:0xf
	s_nop 1
	v_max_f32_dpp v8, v8, v8 row_shr:2 row_mask:0xf bank_mask:0xf
	s_nop 1
	v_max_f32_dpp v8, v8, v8 row_shr:4 row_mask:0xf bank_mask:0xf
	s_nop 1
	v_max_f32_dpp v8, v8, v8 row_shr:8 row_mask:0xf bank_mask:0xf
	s_nop 1
	v_max_f32_dpp v8, v8, v8 row_bcast:15 row_mask:0xa bank_mask:0xf
	s_nop 1
	v_max_f32_dpp v8, v8, v8 row_bcast:31 row_mask:0xc bank_mask:0xf
	s_nop 0
	v_readlane_b32 s22, v8, 63
	s_nop 0
	s_nop 0
	v_cmp_eq_f32_e32 vcc, s22, v1
	s_ff1_i32_b64 s22, vcc
	v_cmp_eq_u32_e32 vcc, s22, v198
	s_nop 1
	v_cndmask_b32_e32 v1, v1, v115, vcc
	v_cndmask_b32_e64 v4, v4, 1, vcc
	s_nop 0
	v_mov_b32_e32 v8, v1
	v_max_f32_dpp v8, v1, v8 row_shr:1 row_mask:0xf bank_mask:0xf
	s_nop 1
	v_max_f32_dpp v8, v8, v8 row_shr:2 row_mask:0xf bank_mask:0xf
	s_nop 1
	v_max_f32_dpp v8, v8, v8 row_shr:4 row_mask:0xf bank_mask:0xf
	s_nop 1
	v_max_f32_dpp v8, v8, v8 row_shr:8 row_mask:0xf bank_mask:0xf
	s_nop 1
	v_max_f32_dpp v8, v8, v8 row_bcast:15 row_mask:0xa bank_mask:0xf
	s_nop 1
	v_max_f32_dpp v8, v8, v8 row_bcast:31 row_mask:0xc bank_mask:0xf
	s_nop 0
	v_readlane_b32 s22, v8, 63
	s_nop 0
	s_nop 0
	v_cmp_eq_f32_e32 vcc, s22, v1
	s_ff1_i32_b64 s22, vcc
	v_cmp_eq_u32_e32 vcc, s22, v198
	s_nop 1
	v_cndmask_b32_e32 v1, v1, v115, vcc
	v_cndmask_b32_e64 v4, v4, 2, vcc
	s_nop 0
	v_mov_b32_e32 v8, v1
	v_max_f32_dpp v8, v1, v8 row_shr:1 row_mask:0xf bank_mask:0xf
	s_nop 1
	v_max_f32_dpp v8, v8, v8 row_shr:2 row_mask:0xf bank_mask:0xf
	s_nop 1
	v_max_f32_dpp v8, v8, v8 row_shr:4 row_mask:0xf bank_mask:0xf
	s_nop 1
	v_max_f32_dpp v8, v8, v8 row_shr:8 row_mask:0xf bank_mask:0xf
	s_nop 1
	v_max_f32_dpp v8, v8, v8 row_bcast:15 row_mask:0xa bank_mask:0xf
	s_nop 1
	v_max_f32_dpp v8, v8, v8 row_bcast:31 row_mask:0xc bank_mask:0xf
	s_nop 0
	v_readlane_b32 s22, v8, 63
	s_nop 0
	s_nop 0
	v_cmp_eq_f32_e32 vcc, s22, v1
	s_ff1_i32_b64 s22, vcc
	v_cmp_eq_u32_e32 vcc, s22, v198
	s_nop 1
	v_cndmask_b32_e32 v1, v1, v115, vcc
	v_cndmask_b32_e64 v4, v4, 3, vcc
	s_nop 0
	v_mov_b32_e32 v8, v1
	v_max_f32_dpp v8, v1, v8 row_shr:1 row_mask:0xf bank_mask:0xf
	s_nop 1
	v_max_f32_dpp v8, v8, v8 row_shr:2 row_mask:0xf bank_mask:0xf
	s_nop 1
	v_max_f32_dpp v8, v8, v8 row_shr:4 row_mask:0xf bank_mask:0xf
	s_nop 1
	v_max_f32_dpp v8, v8, v8 row_shr:8 row_mask:0xf bank_mask:0xf
	s_nop 1
	v_max_f32_dpp v8, v8, v8 row_bcast:15 row_mask:0xa bank_mask:0xf
	s_nop 1
	v_max_f32_dpp v8, v8, v8 row_bcast:31 row_mask:0xc bank_mask:0xf
	s_nop 0
	v_readlane_b32 s22, v8, 63
	v_mov_b32_e32 v8, 0xff800000
	s_nop 0
	v_cmp_eq_f32_e32 vcc, s22, v1
	s_ff1_i32_b64 s22, vcc
	v_cmp_eq_u32_e32 vcc, s22, v198
	s_nop 1
	v_cndmask_b32_e32 v1, v1, v115, vcc
	v_max_f32_e32 v9, v1, v1
	v_cndmask_b32_e64 v4, v4, 4, vcc
	v_mov_b32_dpp v8, v1 row_shr:1 row_mask:0xf bank_mask:0xf
	v_max_f32_e32 v8, v8, v8
	v_max_f32_e32 v8, v9, v8
	s_nop 1
	v_max_f32_dpp v8, v8, v8 row_shr:2 row_mask:0xf bank_mask:0xf
	s_nop 1
	v_max_f32_dpp v8, v8, v8 row_shr:4 row_mask:0xf bank_mask:0xf
	s_nop 1
	v_max_f32_dpp v8, v8, v8 row_shr:8 row_mask:0xf bank_mask:0xf
	s_nop 1
	v_max_f32_dpp v8, v8, v8 row_bcast:15 row_mask:0xa bank_mask:0xf
	s_nop 1
	v_max_f32_dpp v8, v8, v8 row_bcast:31 row_mask:0xc bank_mask:0xf
	s_nop 0
	v_readlane_b32 s22, v8, 63
	v_mov_b32_e32 v8, 0xff800000
	s_nop 0
	v_cmp_eq_f32_e32 vcc, s22, v1
	s_ff1_i32_b64 s22, vcc
	v_cmp_eq_u32_e32 vcc, s22, v198
	s_nop 1
	v_cndmask_b32_e32 v1, v1, v115, vcc
	v_max_f32_e32 v9, v1, v1
	v_cndmask_b32_e64 v4, v4, 5, vcc
	v_mov_b32_dpp v8, v1 row_shr:1 row_mask:0xf bank_mask:0xf
	v_max_f32_e32 v8, v8, v8
	v_max_f32_e32 v8, v9, v8
	s_nop 1
	v_max_f32_dpp v8, v8, v8 row_shr:2 row_mask:0xf bank_mask:0xf
	s_nop 1
	v_max_f32_dpp v8, v8, v8 row_shr:4 row_mask:0xf bank_mask:0xf
	s_nop 1
	v_max_f32_dpp v8, v8, v8 row_shr:8 row_mask:0xf bank_mask:0xf
	s_nop 1
	v_max_f32_dpp v8, v8, v8 row_bcast:15 row_mask:0xa bank_mask:0xf
	s_nop 1
	v_max_f32_dpp v8, v8, v8 row_bcast:31 row_mask:0xc bank_mask:0xf
	s_nop 0
	v_readlane_b32 s22, v8, 63
	v_mov_b32_e32 v8, 0xff800000
	s_nop 0
	v_cmp_eq_f32_e32 vcc, s22, v1
	s_ff1_i32_b64 s22, vcc
	v_cmp_eq_u32_e32 vcc, s22, v198
	s_nop 1
	v_cndmask_b32_e32 v1, v1, v115, vcc
	v_max_f32_e32 v9, v1, v1
	v_cndmask_b32_e64 v4, v4, 6, vcc
	v_mov_b32_dpp v8, v1 row_shr:1 row_mask:0xf bank_mask:0xf
	v_max_f32_e32 v8, v8, v8
	v_max_f32_e32 v8, v9, v8
	s_nop 1
	v_max_f32_dpp v8, v8, v8 row_shr:2 row_mask:0xf bank_mask:0xf
	s_nop 1
	v_max_f32_dpp v8, v8, v8 row_shr:4 row_mask:0xf bank_mask:0xf
	s_nop 1
	v_max_f32_dpp v8, v8, v8 row_shr:8 row_mask:0xf bank_mask:0xf
	s_nop 1
	v_max_f32_dpp v8, v8, v8 row_bcast:15 row_mask:0xa bank_mask:0xf
	s_nop 1
	v_max_f32_dpp v8, v8, v8 row_bcast:31 row_mask:0xc bank_mask:0xf
	s_nop 0
	v_readlane_b32 s22, v8, 63
	s_nop 1
	v_cmp_eq_f32_e32 vcc, s22, v1
	s_ff1_i32_b64 s22, vcc
	v_cmp_ne_u32_e32 vcc, s22, v198
	s_nop 1
	v_cndmask_b32_e32 v8, 7, v4, vcc
	v_cmp_lt_i32_e64 s[22:23], -1, v8
	v_mov_b32_e32 v4, 0
	s_nop 0
	v_cndmask_b32_e64 v1, 0, v7, s[22:23]
	s_nop 1
	v_add_f32_dpp v1, v1, v1 row_shr:1 row_mask:0xf bank_mask:0xf bound_ctrl:1
	s_nop 1
	v_add_f32_dpp v1, v1, v1 row_shr:2 row_mask:0xf bank_mask:0xf bound_ctrl:1
	s_nop 1
	v_add_f32_dpp v1, v1, v1 row_shr:4 row_mask:0xf bank_mask:0xf bound_ctrl:1
	s_nop 1
	v_add_f32_dpp v1, v1, v1 row_shr:8 row_mask:0xf bank_mask:0xf bound_ctrl:1
	s_nop 1
	v_mov_b32_dpp v4, v1 row_bcast:15 row_mask:0xa bank_mask:0xf
	v_add_f32_e32 v1, v1, v4
	v_mov_b32_e32 v4, 0
	s_nop 1
	v_mov_b32_dpp v4, v1 row_bcast:31 row_mask:0xc bank_mask:0xf
	v_add_f32_e32 v1, v1, v4
	s_nop 0
	v_readlane_b32 s43, v1, 63
	v_mov_b32_e32 v1, s35
	s_and_saveexec_b64 s[24:25], s[22:23]
	ds_add_rtn_u32 v1, v101, v116
	s_or_b64 exec, exec, s[24:25]
	ds_read_b32 v4, v119 offset:512
	s_waitcnt lgkmcnt(0)
	v_mul_f32_e32 v4, 0xbfb8aa3b, v4
	v_exp_f32_e32 v4, v4
	s_nop 0
	v_add_f32_e32 v4, 1.0, v4
	v_div_scale_f32 v9, s[24:25], v4, v4, 1.0
	v_rcp_f32_e32 v10, v9
	v_div_scale_f32 v11, vcc, 1.0, v4, 1.0
	v_fma_f32 v12, -v9, v10, 1.0
	v_fmac_f32_e32 v10, v12, v10
	v_mul_f32_e32 v12, v11, v10
	v_fma_f32 v13, -v9, v12, v11
	v_fmac_f32_e32 v12, v13, v10
	v_fma_f32 v9, -v9, v12, v11
	v_div_fmas_f32 v9, v9, v10, v12
	v_div_fixup_f32 v9, v9, v4, 1.0
	v_add_f32_e32 v4, v3, v9
	s_nop 1
	v_max_f32_dpp v10, v4, v4 quad_perm:[1,0,3,2] row_mask:0xf bank_mask:0xf bound_ctrl:1
	s_nop 1
	v_max_f32_dpp v10, v10, v10 quad_perm:[2,3,0,1] row_mask:0xf bank_mask:0xf bound_ctrl:1
	s_nop 1
	v_max_f32_dpp v10, v10, v10 row_half_mirror row_mask:0xf bank_mask:0xf bound_ctrl:1
	v_cmp_eq_f32_e32 vcc, v4, v10
	s_nop 1
	v_and_b32_e32 v11, vcc_hi, v63
	v_and_b32_e32 v12, vcc_lo, v62
	v_ffbl_b32_e32 v11, v11
	v_ffbl_b32_e32 v12, v12
	v_add_u32_e32 v11, 32, v11
	v_min_u32_e32 v11, v12, v11
	v_cmp_ne_u32_e32 vcc, v198, v11
	s_nop 1
	v_cndmask_b32_e32 v11, v115, v4, vcc
	s_nop 1
	v_max_f32_dpp v11, v11, v11 quad_perm:[1,0,3,2] row_mask:0xf bank_mask:0xf bound_ctrl:1
	s_nop 1
	v_max_f32_dpp v11, v11, v11 quad_perm:[2,3,0,1] row_mask:0xf bank_mask:0xf bound_ctrl:1
	s_nop 1
	v_max_f32_dpp v11, v11, v11 row_half_mirror row_mask:0xf bank_mask:0xf bound_ctrl:1
	v_add_f32_e32 v10, v10, v11
	s_nop 0
	v_readlane_b32 s24, v10, 0
	v_readlane_b32 s26, v10, 8
	s_nop 0
	v_cmp_gt_f32_e32 vcc, s24, v10
	v_cmp_eq_f32_e64 s[24:25], s24, v10
	s_and_b64 s[24:25], s[24:25], s[6:7]
	s_or_b64 s[24:25], vcc, s[24:25]
	v_cndmask_b32_e64 v11, 0, 1, s[24:25]
	v_cmp_eq_f32_e64 s[24:25], s26, v10
	v_cmp_gt_f32_e32 vcc, s26, v10
	s_and_b64 s[24:25], s[24:25], s[8:9]
	s_or_b64 s[24:25], vcc, s[24:25]
	v_cndmask_b32_e64 v12, 0, 1, s[24:25]
	v_readlane_b32 s24, v10, 16
	s_nop 1
	v_cmp_gt_f32_e32 vcc, s24, v10
	v_cmp_eq_f32_e64 s[24:25], s24, v10
	s_and_b64 s[24:25], s[24:25], s[10:11]
	s_or_b64 s[24:25], vcc, s[24:25]
	v_cndmask_b32_e64 v13, 0, 1, s[24:25]
	v_readlane_b32 s24, v10, 24
	v_add3_u32 v11, v11, v12, v13
	s_nop 0
	v_cmp_gt_f32_e32 vcc, s24, v10
	v_cmp_eq_f32_e64 s[24:25], s24, v10
	s_and_b64 s[24:25], s[24:25], s[12:13]
	s_or_b64 s[24:25], vcc, s[24:25]
	v_cndmask_b32_e64 v12, 0, 1, s[24:25]
	v_readlane_b32 s24, v10, 32
	s_nop 1
	v_cmp_gt_f32_e32 vcc, s24, v10
	v_cmp_eq_f32_e64 s[24:25], s24, v10
	s_and_b64 s[24:25], s[24:25], s[14:15]
	s_or_b64 s[24:25], vcc, s[24:25]
	v_cndmask_b32_e64 v13, 0, 1, s[24:25]
	v_readlane_b32 s24, v10, 40
	v_add3_u32 v11, v11, v12, v13
	s_nop 0
	v_cmp_gt_f32_e32 vcc, s24, v10
	v_cmp_eq_f32_e64 s[24:25], s24, v10
	s_and_b64 s[24:25], s[24:25], s[16:17]
	s_or_b64 s[24:25], vcc, s[24:25]
	v_cndmask_b32_e64 v12, 0, 1, s[24:25]
	v_readlane_b32 s24, v10, 48
	s_nop 1
	v_cmp_gt_f32_e32 vcc, s24, v10
	v_cmp_eq_f32_e64 s[24:25], s24, v10
	s_and_b64 s[24:25], s[18:19], s[24:25]
	s_or_b64 s[24:25], vcc, s[24:25]
	v_cndmask_b32_e64 v13, 0, 1, s[24:25]
	v_readlane_b32 s24, v10, 56
	s_nop 1
	v_cmp_gt_f32_e32 vcc, s24, v10
	s_nop 1
	v_addc_co_u32_e32 v10, vcc, v11, v12, vcc
	v_add_u32_e32 v10, v10, v13
	v_cmp_gt_u32_e32 vcc, 4, v10
	s_nop 0
	s_nop 0
	v_cndmask_b32_e32 v4, v115, v4, vcc
	s_nop 0
	v_mov_b32_e32 v10, v4
	v_max_f32_dpp v10, v4, v10 row_shr:1 row_mask:0xf bank_mask:0xf
	s_nop 1
	v_max_f32_dpp v10, v10, v10 row_shr:2 row_mask:0xf bank_mask:0xf
	s_nop 1
	v_max_f32_dpp v10, v10, v10 row_shr:4 row_mask:0xf bank_mask:0xf
	s_nop 1
	v_max_f32_dpp v10, v10, v10 row_shr:8 row_mask:0xf bank_mask:0xf
	s_nop 1
	v_max_f32_dpp v10, v10, v10 row_bcast:15 row_mask:0xa bank_mask:0xf
	s_nop 1
	v_max_f32_dpp v10, v10, v10 row_bcast:31 row_mask:0xc bank_mask:0xf
	s_nop 0
	v_readlane_b32 s24, v10, 63
	s_nop 1
	v_cmp_eq_f32_e32 vcc, s24, v4
	s_ff1_i32_b64 s24, vcc
	v_cmp_ne_u32_e32 vcc, s24, v198
	s_nop 1
	v_cndmask_b32_e32 v4, v115, v4, vcc
	v_cndmask_b32_e64 v10, 0, -1, vcc
	s_nop 0
	v_mov_b32_e32 v11, v4
	v_max_f32_dpp v11, v4, v11 row_shr:1 row_mask:0xf bank_mask:0xf
	s_nop 1
	v_max_f32_dpp v11, v11, v11 row_shr:2 row_mask:0xf bank_mask:0xf
	s_nop 1
	v_max_f32_dpp v11, v11, v11 row_shr:4 row_mask:0xf bank_mask:0xf
	s_nop 1
	v_max_f32_dpp v11, v11, v11 row_shr:8 row_mask:0xf bank_mask:0xf
	s_nop 1
	v_max_f32_dpp v11, v11, v11 row_bcast:15 row_mask:0xa bank_mask:0xf
	s_nop 1
	v_max_f32_dpp v11, v11, v11 row_bcast:31 row_mask:0xc bank_mask:0xf
	s_nop 0
	v_readlane_b32 s24, v11, 63
	s_nop 0
	s_nop 0
	v_cmp_eq_f32_e32 vcc, s24, v4
	s_ff1_i32_b64 s24, vcc
	v_cmp_eq_u32_e32 vcc, s24, v198
	s_nop 1
	v_cndmask_b32_e32 v4, v4, v115, vcc
	v_cndmask_b32_e64 v10, v10, 1, vcc
	s_nop 0
	v_mov_b32_e32 v11, v4
	v_max_f32_dpp v11, v4, v11 row_shr:1 row_mask:0xf bank_mask:0xf
	s_nop 1
	v_max_f32_dpp v11, v11, v11 row_shr:2 row_mask:0xf bank_mask:0xf
	s_nop 1
	v_max_f32_dpp v11, v11, v11 row_shr:4 row_mask:0xf bank_mask:0xf
	s_nop 1
	v_max_f32_dpp v11, v11, v11 row_shr:8 row_mask:0xf bank_mask:0xf
	s_nop 1
	v_max_f32_dpp v11, v11, v11 row_bcast:15 row_mask:0xa bank_mask:0xf
	s_nop 1
	v_max_f32_dpp v11, v11, v11 row_bcast:31 row_mask:0xc bank_mask:0xf
	s_nop 0
	v_readlane_b32 s24, v11, 63
	s_nop 0
	s_nop 0
	v_cmp_eq_f32_e32 vcc, s24, v4
	s_ff1_i32_b64 s24, vcc
	v_cmp_eq_u32_e32 vcc, s24, v198
	s_nop 1
	v_cndmask_b32_e32 v4, v4, v115, vcc
	v_cndmask_b32_e64 v10, v10, 2, vcc
	s_nop 0
	v_mov_b32_e32 v11, v4
	v_max_f32_dpp v11, v4, v11 row_shr:1 row_mask:0xf bank_mask:0xf
	s_nop 1
	v_max_f32_dpp v11, v11, v11 row_shr:2 row_mask:0xf bank_mask:0xf
	s_nop 1
	v_max_f32_dpp v11, v11, v11 row_shr:4 row_mask:0xf bank_mask:0xf
	s_nop 1
	v_max_f32_dpp v11, v11, v11 row_shr:8 row_mask:0xf bank_mask:0xf
	s_nop 1
	v_max_f32_dpp v11, v11, v11 row_bcast:15 row_mask:0xa bank_mask:0xf
	s_nop 1
	v_max_f32_dpp v11, v11, v11 row_bcast:31 row_mask:0xc bank_mask:0xf
	s_nop 0
	v_readlane_b32 s24, v11, 63
	s_nop 0
	s_nop 0
	v_cmp_eq_f32_e32 vcc, s24, v4
	s_ff1_i32_b64 s24, vcc
	v_cmp_eq_u32_e32 vcc, s24, v198
	s_nop 1
	v_cndmask_b32_e32 v4, v4, v115, vcc
	v_cndmask_b32_e64 v10, v10, 3, vcc
	s_nop 0
	v_mov_b32_e32 v11, v4
	v_max_f32_dpp v11, v4, v11 row_shr:1 row_mask:0xf bank_mask:0xf
	s_nop 1
	v_max_f32_dpp v11, v11, v11 row_shr:2 row_mask:0xf bank_mask:0xf
	s_nop 1
	v_max_f32_dpp v11, v11, v11 row_shr:4 row_mask:0xf bank_mask:0xf
	s_nop 1
	v_max_f32_dpp v11, v11, v11 row_shr:8 row_mask:0xf bank_mask:0xf
	s_nop 1
	v_max_f32_dpp v11, v11, v11 row_bcast:15 row_mask:0xa bank_mask:0xf
	s_nop 1
	v_max_f32_dpp v11, v11, v11 row_bcast:31 row_mask:0xc bank_mask:0xf
	s_nop 0
	v_readlane_b32 s24, v11, 63
	v_mov_b32_e32 v11, 0xff800000
	s_nop 0
	v_cmp_eq_f32_e32 vcc, s24, v4
	s_ff1_i32_b64 s24, vcc
	v_cmp_eq_u32_e32 vcc, s24, v198
	s_nop 1
	v_cndmask_b32_e32 v4, v4, v115, vcc
	v_max_f32_e32 v12, v4, v4
	v_cndmask_b32_e64 v10, v10, 4, vcc
	v_mov_b32_dpp v11, v4 row_shr:1 row_mask:0xf bank_mask:0xf
	v_max_f32_e32 v11, v11, v11
	v_max_f32_e32 v11, v12, v11
	s_nop 1
	v_max_f32_dpp v11, v11, v11 row_shr:2 row_mask:0xf bank_mask:0xf
	s_nop 1
	v_max_f32_dpp v11, v11, v11 row_shr:4 row_mask:0xf bank_mask:0xf
	s_nop 1
	v_max_f32_dpp v11, v11, v11 row_shr:8 row_mask:0xf bank_mask:0xf
	s_nop 1
	v_max_f32_dpp v11, v11, v11 row_bcast:15 row_mask:0xa bank_mask:0xf
	s_nop 1
	v_max_f32_dpp v11, v11, v11 row_bcast:31 row_mask:0xc bank_mask:0xf
	s_nop 0
	v_readlane_b32 s24, v11, 63
	v_mov_b32_e32 v11, 0xff800000
	s_nop 0
	v_cmp_eq_f32_e32 vcc, s24, v4
	s_ff1_i32_b64 s24, vcc
	v_cmp_eq_u32_e32 vcc, s24, v198
	s_nop 1
	v_cndmask_b32_e32 v4, v4, v115, vcc
	v_max_f32_e32 v12, v4, v4
	v_cndmask_b32_e64 v10, v10, 5, vcc
	v_mov_b32_dpp v11, v4 row_shr:1 row_mask:0xf bank_mask:0xf
	v_max_f32_e32 v11, v11, v11
	v_max_f32_e32 v11, v12, v11
	s_nop 1
	v_max_f32_dpp v11, v11, v11 row_shr:2 row_mask:0xf bank_mask:0xf
	s_nop 1
	v_max_f32_dpp v11, v11, v11 row_shr:4 row_mask:0xf bank_mask:0xf
	s_nop 1
	v_max_f32_dpp v11, v11, v11 row_shr:8 row_mask:0xf bank_mask:0xf
	s_nop 1
	v_max_f32_dpp v11, v11, v11 row_bcast:15 row_mask:0xa bank_mask:0xf
	s_nop 1
	v_max_f32_dpp v11, v11, v11 row_bcast:31 row_mask:0xc bank_mask:0xf
	s_nop 0
	v_readlane_b32 s24, v11, 63
	v_mov_b32_e32 v11, 0xff800000
	s_nop 0
	v_cmp_eq_f32_e32 vcc, s24, v4
	s_ff1_i32_b64 s24, vcc
	v_cmp_eq_u32_e32 vcc, s24, v198
	s_nop 1
	v_cndmask_b32_e32 v4, v4, v115, vcc
	v_max_f32_e32 v12, v4, v4
	v_cndmask_b32_e64 v10, v10, 6, vcc
	v_mov_b32_dpp v11, v4 row_shr:1 row_mask:0xf bank_mask:0xf
	v_max_f32_e32 v11, v11, v11
	v_max_f32_e32 v11, v12, v11
	s_nop 1
	v_max_f32_dpp v11, v11, v11 row_shr:2 row_mask:0xf bank_mask:0xf
	s_nop 1
	v_max_f32_dpp v11, v11, v11 row_shr:4 row_mask:0xf bank_mask:0xf
	s_nop 1
	v_max_f32_dpp v11, v11, v11 row_shr:8 row_mask:0xf bank_mask:0xf
	s_nop 1
	v_max_f32_dpp v11, v11, v11 row_bcast:15 row_mask:0xa bank_mask:0xf
	s_nop 1
	v_max_f32_dpp v11, v11, v11 row_bcast:31 row_mask:0xc bank_mask:0xf
	s_nop 0
	v_readlane_b32 s24, v11, 63
	v_mov_b32_e32 v11, 0
	s_nop 0
	v_cmp_eq_f32_e32 vcc, s24, v4
	s_ff1_i32_b64 s24, vcc
	v_cmp_ne_u32_e32 vcc, s24, v198
	s_nop 1
	v_cndmask_b32_e32 v10, 7, v10, vcc
	v_cmp_lt_i32_e64 s[24:25], -1, v10
	s_nop 1
	v_cndmask_b32_e64 v4, 0, v9, s[24:25]
	s_nop 1
	v_add_f32_dpp v4, v4, v4 row_shr:1 row_mask:0xf bank_mask:0xf bound_ctrl:1
	s_nop 1
	v_add_f32_dpp v4, v4, v4 row_shr:2 row_mask:0xf bank_mask:0xf bound_ctrl:1
	s_nop 1
	v_add_f32_dpp v4, v4, v4 row_shr:4 row_mask:0xf bank_mask:0xf bound_ctrl:1
	s_nop 1
	v_add_f32_dpp v4, v4, v4 row_shr:8 row_mask:0xf bank_mask:0xf bound_ctrl:1
	s_nop 1
	v_mov_b32_dpp v11, v4 row_bcast:15 row_mask:0xa bank_mask:0xf
	v_add_f32_e32 v4, v4, v11
	v_mov_b32_e32 v11, 0
	s_nop 1
	v_mov_b32_dpp v11, v4 row_bcast:31 row_mask:0xc bank_mask:0xf
	v_add_f32_e32 v4, v4, v11
	s_nop 0
	v_readlane_b32 s45, v4, 63
	v_mov_b32_e32 v4, s35
	s_and_saveexec_b64 s[26:27], s[24:25]
	ds_add_rtn_u32 v4, v101, v116
	s_or_b64 exec, exec, s[26:27]
	ds_read_b32 v11, v119 offset:768
	s_waitcnt lgkmcnt(0)
	v_mul_f32_e32 v11, 0xbfb8aa3b, v11
	v_exp_f32_e32 v11, v11
	s_nop 0
	v_add_f32_e32 v11, 1.0, v11
	v_div_scale_f32 v12, s[26:27], v11, v11, 1.0
	v_rcp_f32_e32 v13, v12
	v_div_scale_f32 v14, vcc, 1.0, v11, 1.0
	v_fma_f32 v15, -v12, v13, 1.0
	v_fmac_f32_e32 v13, v15, v13
	v_mul_f32_e32 v15, v14, v13
	v_fma_f32 v16, -v12, v15, v14
	v_fmac_f32_e32 v15, v16, v13
	v_fma_f32 v12, -v12, v15, v14
	v_div_fmas_f32 v12, v12, v13, v15
	v_div_fixup_f32 v11, v12, v11, 1.0
	v_add_f32_e32 v3, v3, v11
	s_nop 1
	v_max_f32_dpp v12, v3, v3 quad_perm:[1,0,3,2] row_mask:0xf bank_mask:0xf bound_ctrl:1
	s_nop 1
	v_max_f32_dpp v12, v12, v12 quad_perm:[2,3,0,1] row_mask:0xf bank_mask:0xf bound_ctrl:1
	s_nop 1
	v_max_f32_dpp v12, v12, v12 row_half_mirror row_mask:0xf bank_mask:0xf bound_ctrl:1
	v_cmp_eq_f32_e32 vcc, v3, v12
	s_nop 1
	v_and_b32_e32 v13, vcc_hi, v63
	v_and_b32_e32 v14, vcc_lo, v62
	v_ffbl_b32_e32 v13, v13
	v_ffbl_b32_e32 v14, v14
	v_add_u32_e32 v13, 32, v13
	v_min_u32_e32 v13, v14, v13
	v_cmp_ne_u32_e32 vcc, v198, v13
	s_nop 1
	v_cndmask_b32_e32 v13, v115, v3, vcc
	s_nop 1
	v_max_f32_dpp v13, v13, v13 quad_perm:[1,0,3,2] row_mask:0xf bank_mask:0xf bound_ctrl:1
	s_nop 1
	v_max_f32_dpp v13, v13, v13 quad_perm:[2,3,0,1] row_mask:0xf bank_mask:0xf bound_ctrl:1
	s_nop 1
	v_max_f32_dpp v13, v13, v13 row_half_mirror row_mask:0xf bank_mask:0xf bound_ctrl:1
	v_add_f32_e32 v12, v12, v13
	s_nop 0
	v_readlane_b32 s26, v12, 0
	v_readlane_b32 s47, v12, 8
	s_nop 0
	v_cmp_gt_f32_e32 vcc, s26, v12
	v_cmp_eq_f32_e64 s[26:27], s26, v12
	s_and_b64 s[26:27], s[26:27], s[6:7]
	s_or_b64 s[26:27], vcc, s[26:27]
	v_cndmask_b32_e64 v13, 0, 1, s[26:27]
	v_cmp_eq_f32_e64 s[26:27], s47, v12
	v_cmp_gt_f32_e32 vcc, s47, v12
	s_and_b64 s[26:27], s[26:27], s[8:9]
	s_or_b64 s[26:27], vcc, s[26:27]
	v_cndmask_b32_e64 v14, 0, 1, s[26:27]
	v_readlane_b32 s26, v12, 16
	s_nop 1
	v_cmp_gt_f32_e32 vcc, s26, v12
	v_cmp_eq_f32_e64 s[26:27], s26, v12
	s_and_b64 s[26:27], s[26:27], s[10:11]
	s_or_b64 s[26:27], vcc, s[26:27]
	v_cndmask_b32_e64 v15, 0, 1, s[26:27]
	v_readlane_b32 s26, v12, 24
	v_add3_u32 v13, v13, v14, v15
	s_nop 0
	v_cmp_gt_f32_e32 vcc, s26, v12
	v_cmp_eq_f32_e64 s[26:27], s26, v12
	s_and_b64 s[26:27], s[26:27], s[12:13]
	s_or_b64 s[26:27], vcc, s[26:27]
	v_cndmask_b32_e64 v14, 0, 1, s[26:27]
	v_readlane_b32 s26, v12, 32
	s_nop 1
	v_cmp_gt_f32_e32 vcc, s26, v12
	v_cmp_eq_f32_e64 s[26:27], s26, v12
	s_and_b64 s[26:27], s[26:27], s[14:15]
	s_or_b64 s[26:27], vcc, s[26:27]
	v_cndmask_b32_e64 v15, 0, 1, s[26:27]
	v_readlane_b32 s26, v12, 40
	v_add3_u32 v13, v13, v14, v15
	s_nop 0
	v_cmp_gt_f32_e32 vcc, s26, v12
	v_cmp_eq_f32_e64 s[26:27], s26, v12
	s_and_b64 s[26:27], s[26:27], s[16:17]
	s_or_b64 s[26:27], vcc, s[26:27]
	v_cndmask_b32_e64 v14, 0, 1, s[26:27]
	v_readlane_b32 s26, v12, 48
	s_nop 1
	v_cmp_gt_f32_e32 vcc, s26, v12
	v_cmp_eq_f32_e64 s[26:27], s26, v12
	s_and_b64 s[26:27], s[18:19], s[26:27]
	s_or_b64 s[26:27], vcc, s[26:27]
	v_cndmask_b32_e64 v15, 0, 1, s[26:27]
	v_readlane_b32 s26, v12, 56
	s_nop 1
	v_cmp_gt_f32_e32 vcc, s26, v12
	s_nop 1
	v_addc_co_u32_e32 v12, vcc, v13, v14, vcc
	v_add_u32_e32 v12, v12, v15
	v_cmp_gt_u32_e32 vcc, 4, v12
	s_nop 0
	s_nop 0
	v_cndmask_b32_e32 v3, v115, v3, vcc
	s_nop 0
	v_mov_b32_e32 v12, v3
	v_max_f32_dpp v12, v3, v12 row_shr:1 row_mask:0xf bank_mask:0xf
	s_nop 1
	v_max_f32_dpp v12, v12, v12 row_shr:2 row_mask:0xf bank_mask:0xf
	s_nop 1
	v_max_f32_dpp v12, v12, v12 row_shr:4 row_mask:0xf bank_mask:0xf
	s_nop 1
	v_max_f32_dpp v12, v12, v12 row_shr:8 row_mask:0xf bank_mask:0xf
	s_nop 1
	v_max_f32_dpp v12, v12, v12 row_bcast:15 row_mask:0xa bank_mask:0xf
	s_nop 1
	v_max_f32_dpp v12, v12, v12 row_bcast:31 row_mask:0xc bank_mask:0xf
	s_nop 0
	v_readlane_b32 s26, v12, 63
	s_nop 1
	v_cmp_eq_f32_e32 vcc, s26, v3
	s_ff1_i32_b64 s26, vcc
	v_cmp_ne_u32_e32 vcc, s26, v198
	s_nop 1
	v_cndmask_b32_e32 v3, v115, v3, vcc
	v_cndmask_b32_e64 v12, 0, -1, vcc
	s_nop 0
	v_mov_b32_e32 v13, v3
	v_max_f32_dpp v13, v3, v13 row_shr:1 row_mask:0xf bank_mask:0xf
	s_nop 1
	v_max_f32_dpp v13, v13, v13 row_shr:2 row_mask:0xf bank_mask:0xf
	s_nop 1
	v_max_f32_dpp v13, v13, v13 row_shr:4 row_mask:0xf bank_mask:0xf
	s_nop 1
	v_max_f32_dpp v13, v13, v13 row_shr:8 row_mask:0xf bank_mask:0xf
	s_nop 1
	v_max_f32_dpp v13, v13, v13 row_bcast:15 row_mask:0xa bank_mask:0xf
	s_nop 1
	v_max_f32_dpp v13, v13, v13 row_bcast:31 row_mask:0xc bank_mask:0xf
	s_nop 0
	v_readlane_b32 s26, v13, 63
	s_nop 0
	s_nop 0
	v_cmp_eq_f32_e32 vcc, s26, v3
	s_ff1_i32_b64 s26, vcc
	v_cmp_eq_u32_e32 vcc, s26, v198
	s_nop 1
	v_cndmask_b32_e32 v3, v3, v115, vcc
	v_cndmask_b32_e64 v12, v12, 1, vcc
	s_nop 0
	v_mov_b32_e32 v13, v3
	v_max_f32_dpp v13, v3, v13 row_shr:1 row_mask:0xf bank_mask:0xf
	s_nop 1
	v_max_f32_dpp v13, v13, v13 row_shr:2 row_mask:0xf bank_mask:0xf
	s_nop 1
	v_max_f32_dpp v13, v13, v13 row_shr:4 row_mask:0xf bank_mask:0xf
	s_nop 1
	v_max_f32_dpp v13, v13, v13 row_shr:8 row_mask:0xf bank_mask:0xf
	s_nop 1
	v_max_f32_dpp v13, v13, v13 row_bcast:15 row_mask:0xa bank_mask:0xf
	s_nop 1
	v_max_f32_dpp v13, v13, v13 row_bcast:31 row_mask:0xc bank_mask:0xf
	s_nop 0
	v_readlane_b32 s26, v13, 63
	s_nop 0
	s_nop 0
	v_cmp_eq_f32_e32 vcc, s26, v3
	s_ff1_i32_b64 s26, vcc
	v_cmp_eq_u32_e32 vcc, s26, v198
	s_nop 1
	v_cndmask_b32_e32 v3, v3, v115, vcc
	v_cndmask_b32_e64 v12, v12, 2, vcc
	s_nop 0
	v_mov_b32_e32 v13, v3
	v_max_f32_dpp v13, v3, v13 row_shr:1 row_mask:0xf bank_mask:0xf
	s_nop 1
	v_max_f32_dpp v13, v13, v13 row_shr:2 row_mask:0xf bank_mask:0xf
	s_nop 1
	v_max_f32_dpp v13, v13, v13 row_shr:4 row_mask:0xf bank_mask:0xf
	s_nop 1
	v_max_f32_dpp v13, v13, v13 row_shr:8 row_mask:0xf bank_mask:0xf
	s_nop 1
	v_max_f32_dpp v13, v13, v13 row_bcast:15 row_mask:0xa bank_mask:0xf
	s_nop 1
	v_max_f32_dpp v13, v13, v13 row_bcast:31 row_mask:0xc bank_mask:0xf
	s_nop 0
	v_readlane_b32 s26, v13, 63
	s_nop 0
	s_nop 0
	v_cmp_eq_f32_e32 vcc, s26, v3
	s_ff1_i32_b64 s26, vcc
	v_cmp_eq_u32_e32 vcc, s26, v198
	s_nop 1
	v_cndmask_b32_e32 v3, v3, v115, vcc
	v_cndmask_b32_e64 v12, v12, 3, vcc
	s_nop 0
	v_mov_b32_e32 v13, v3
	v_max_f32_dpp v13, v3, v13 row_shr:1 row_mask:0xf bank_mask:0xf
	s_nop 1
	v_max_f32_dpp v13, v13, v13 row_shr:2 row_mask:0xf bank_mask:0xf
	s_nop 1
	v_max_f32_dpp v13, v13, v13 row_shr:4 row_mask:0xf bank_mask:0xf
	s_nop 1
	v_max_f32_dpp v13, v13, v13 row_shr:8 row_mask:0xf bank_mask:0xf
	s_nop 1
	v_max_f32_dpp v13, v13, v13 row_bcast:15 row_mask:0xa bank_mask:0xf
	s_nop 1
	v_max_f32_dpp v13, v13, v13 row_bcast:31 row_mask:0xc bank_mask:0xf
	s_nop 0
	v_readlane_b32 s26, v13, 63
	v_mov_b32_e32 v13, 0xff800000
	s_nop 0
	v_cmp_eq_f32_e32 vcc, s26, v3
	s_ff1_i32_b64 s26, vcc
	v_cmp_eq_u32_e32 vcc, s26, v198
	s_nop 1
	v_cndmask_b32_e32 v3, v3, v115, vcc
	v_max_f32_e32 v14, v3, v3
	v_cndmask_b32_e64 v12, v12, 4, vcc
	v_mov_b32_dpp v13, v3 row_shr:1 row_mask:0xf bank_mask:0xf
	v_max_f32_e32 v13, v13, v13
	v_max_f32_e32 v13, v14, v13
	s_nop 1
	v_max_f32_dpp v13, v13, v13 row_shr:2 row_mask:0xf bank_mask:0xf
	s_nop 1
	v_max_f32_dpp v13, v13, v13 row_shr:4 row_mask:0xf bank_mask:0xf
	s_nop 1
	v_max_f32_dpp v13, v13, v13 row_shr:8 row_mask:0xf bank_mask:0xf
	s_nop 1
	v_max_f32_dpp v13, v13, v13 row_bcast:15 row_mask:0xa bank_mask:0xf
	s_nop 1
	v_max_f32_dpp v13, v13, v13 row_bcast:31 row_mask:0xc bank_mask:0xf
	s_nop 0
	v_readlane_b32 s26, v13, 63
	v_mov_b32_e32 v13, 0xff800000
	s_nop 0
	v_cmp_eq_f32_e32 vcc, s26, v3
	s_ff1_i32_b64 s26, vcc
	v_cmp_eq_u32_e32 vcc, s26, v198
	s_nop 1
	v_cndmask_b32_e32 v3, v3, v115, vcc
	v_max_f32_e32 v14, v3, v3
	v_cndmask_b32_e64 v12, v12, 5, vcc
	v_mov_b32_dpp v13, v3 row_shr:1 row_mask:0xf bank_mask:0xf
	v_max_f32_e32 v13, v13, v13
	v_max_f32_e32 v13, v14, v13
	s_nop 1
	v_max_f32_dpp v13, v13, v13 row_shr:2 row_mask:0xf bank_mask:0xf
	s_nop 1
	v_max_f32_dpp v13, v13, v13 row_shr:4 row_mask:0xf bank_mask:0xf
	s_nop 1
	v_max_f32_dpp v13, v13, v13 row_shr:8 row_mask:0xf bank_mask:0xf
	s_nop 1
	v_max_f32_dpp v13, v13, v13 row_bcast:15 row_mask:0xa bank_mask:0xf
	s_nop 1
	v_max_f32_dpp v13, v13, v13 row_bcast:31 row_mask:0xc bank_mask:0xf
	s_nop 0
	v_readlane_b32 s26, v13, 63
	v_mov_b32_e32 v13, 0xff800000
	s_nop 0
	v_cmp_eq_f32_e32 vcc, s26, v3
	s_ff1_i32_b64 s26, vcc
	v_cmp_eq_u32_e32 vcc, s26, v198
	s_nop 1
	v_cndmask_b32_e32 v3, v3, v115, vcc
	v_max_f32_e32 v14, v3, v3
	v_cndmask_b32_e64 v12, v12, 6, vcc
	v_mov_b32_dpp v13, v3 row_shr:1 row_mask:0xf bank_mask:0xf
	v_max_f32_e32 v13, v13, v13
	v_max_f32_e32 v13, v14, v13
	s_nop 1
	v_max_f32_dpp v13, v13, v13 row_shr:2 row_mask:0xf bank_mask:0xf
	s_nop 1
	v_max_f32_dpp v13, v13, v13 row_shr:4 row_mask:0xf bank_mask:0xf
	s_nop 1
	v_max_f32_dpp v13, v13, v13 row_shr:8 row_mask:0xf bank_mask:0xf
	s_nop 1
	v_max_f32_dpp v13, v13, v13 row_bcast:15 row_mask:0xa bank_mask:0xf
	v_mov_b32_e32 v14, 0xff800000
	s_nop 1
	v_max_f32_dpp v13, v13, v13 row_bcast:31 row_mask:0xc bank_mask:0xf
	s_nop 0
	v_readlane_b32 s26, v13, 63
	v_mov_b32_e32 v13, 0
	s_nop 0
	v_cmp_eq_f32_e32 vcc, s26, v3
	s_ff1_i32_b64 s26, vcc
	v_cmp_ne_u32_e32 vcc, s26, v198
	s_nop 1
	v_cndmask_b32_e32 v12, 7, v12, vcc
	v_cmp_lt_i32_e64 s[26:27], -1, v12
	s_nop 1
	v_cndmask_b32_e64 v3, 0, v11, s[26:27]
	s_nop 1
	v_add_f32_dpp v3, v3, v3 row_shr:1 row_mask:0xf bank_mask:0xf bound_ctrl:1
	s_nop 1
	v_add_f32_dpp v3, v3, v3 row_shr:2 row_mask:0xf bank_mask:0xf bound_ctrl:1
	s_nop 1
	v_add_f32_dpp v3, v3, v3 row_shr:4 row_mask:0xf bank_mask:0xf bound_ctrl:1
	s_nop 1
	v_add_f32_dpp v3, v3, v3 row_shr:8 row_mask:0xf bank_mask:0xf bound_ctrl:1
	s_nop 1
	v_mov_b32_dpp v13, v3 row_bcast:15 row_mask:0xa bank_mask:0xf
	v_add_f32_e32 v3, v3, v13
	v_mov_b32_e32 v13, 0
	s_nop 1
	v_mov_b32_dpp v13, v3 row_bcast:31 row_mask:0xc bank_mask:0xf
	v_add_f32_e32 v3, v3, v13
	s_nop 0
	v_readlane_b32 s47, v3, 63
	v_mov_b32_e32 v3, s35
	s_and_saveexec_b64 s[48:49], s[26:27]
	ds_add_rtn_u32 v3, v101, v116
	s_or_b64 exec, exec, s[48:49]
	s_waitcnt lgkmcnt(0)
	s_barrier
	s_and_saveexec_b64 s[48:49], s[0:1]
	s_cbranch_execz .LBB0_2098
	ds_read_b32 v13, v100
	s_waitcnt lgkmcnt(0)
	global_atomic_add v13, v[64:65], v13, off offset:256 sc0
	s_waitcnt vmcnt(0)
	ds_write_b32 v102, v13
